# k_layer<1>/<2>: kernarg s_loads moved ahead of the code-prefetch sequence and entry warm-up ladder so their latency overlaps them
# baseline (speedup 1.0000x reference)
_Z7k_layerILi1EEvPKDF16_PKiPKjS3_S3_S1_PKfPDF16_PhS3_S7_Pf:
	s_load_dwordx2 s[24:25], s[0:1], 0x50
	s_load_dwordx8 s[8:15], s[0:1], 0x0
	s_load_dwordx8 s[16:23], s[0:1], 0x20
	s_getpc_b64 s[4:5]
	v_lshlrev_b32_e32 v116, 6, v0
	s_movk_i32 s6, 0xd0
	v_cmp_gt_u32_e32 vcc, s6, v0
	s_and_saveexec_b64 s[6:7], vcc
	global_load_dword v116, v116, s[4:5]
	s_mov_b64 exec, s[6:7]
	v_readfirstlane_b32 s3, v0
	s_lshr_b32 s3, s3, 6
	s_cmp_eq_u32 s3, 0
	s_cbranch_scc1 .Lic1p_t0
	s_cmp_eq_u32 s3, 1
	s_cbranch_scc1 .Lic1p_t1
	s_cmp_eq_u32 s3, 2
	s_cbranch_scc1 .Lic1p_t2
	s_cmp_eq_u32 s3, 3
	s_cbranch_scc1 .Lic1p_t3
	s_cmp_eq_u32 s3, 4
	s_cbranch_scc1 .Lic1p_t4
	s_cmp_eq_u32 s3, 5
	s_cbranch_scc1 .Lic1p_t5
	s_cmp_eq_u32 s3, 6
	s_cbranch_scc1 .Lic1p_t6
	s_cmp_eq_u32 s3, 7
	s_cbranch_scc1 .Lic1p_t7
	s_cmp_eq_u32 s3, 8
	s_cbranch_scc1 .Lic1p_t8
	s_cmp_eq_u32 s3, 9
	s_cbranch_scc1 .Lic1p_t9
.Lic1p_done:
	v_lshrrev_b32_e32 v2, 5, v0
	v_and_b32_e32 v4, 31, v0
	v_mul_u32_u24_e32 v3, 0x220, v2
	v_lshlrev_b32_e32 v5, 4, v4
	v_or_b32_e32 v1, 0xfffffc00, v0
	v_add3_u32 v4, v3, v5, 0
	v_add_u32_e32 v4, 0x1cd90, v4
	v_lshl_or_b32 v2, v2, 9, v5
	v_mov_b32_e32 v3, 0
	s_branch .Lic1p_s0

_Z7k_layerILi2EEvPKDF16_PKiPKjS3_S3_S1_PKfPDF16_PhS3_S7_Pf:
	s_load_dwordx2 s[24:25], s[0:1], 0x58
	s_load_dwordx4 s[12:15], s[0:1], 0x0
	s_load_dwordx2 s[26:27], s[0:1], 0x10
	s_load_dwordx4 s[16:19], s[0:1], 0x48
	s_load_dwordx4 s[20:23], s[0:1], 0x28
	s_getpc_b64 s[4:5]
	v_lshlrev_b32_e32 v104, 6, v0
	s_movk_i32 s6, 0xe5
	v_cmp_gt_u32_e32 vcc, s6, v0
	s_and_saveexec_b64 s[6:7], vcc
	global_load_dword v104, v104, s[4:5]
	s_mov_b64 exec, s[6:7]
	v_readfirstlane_b32 s3, v0
	s_lshr_b32 s3, s3, 6
	s_cmp_eq_u32 s3, 0
	s_cbranch_scc1 .Lic2p_t0
	s_cmp_eq_u32 s3, 1
	s_cbranch_scc1 .Lic2p_t1
	s_cmp_eq_u32 s3, 2
	s_cbranch_scc1 .Lic2p_t2
	s_cmp_eq_u32 s3, 3
	s_cbranch_scc1 .Lic2p_t3
	s_cmp_eq_u32 s3, 4
	s_cbranch_scc1 .Lic2p_t4
	s_cmp_eq_u32 s3, 5
	s_cbranch_scc1 .Lic2p_t5
	s_cmp_eq_u32 s3, 6
	s_cbranch_scc1 .Lic2p_t6
	s_cmp_eq_u32 s3, 7
	s_cbranch_scc1 .Lic2p_t7
	s_cmp_eq_u32 s3, 8
	s_cbranch_scc1 .Lic2p_t8
	s_cmp_eq_u32 s3, 9
	s_cbranch_scc1 .Lic2p_t9
.Lic2p_done:
	v_lshrrev_b32_e32 v2, 5, v0
	v_and_b32_e32 v4, 31, v0
	v_mul_u32_u24_e32 v3, 0x220, v2
	v_lshlrev_b32_e32 v5, 4, v4
	v_add3_u32 v4, v3, v5, 0
	v_add_u32_e32 v4, 0xcf10, v4
	v_lshl_or_b32 v2, v2, 9, v5
	s_branch .Lic2p_s0
